# FoX (P3) tile loop: packed f32 VALU ops (v_pk_fma/add/mul_f32) beside the MFMAs split into two scalar ops each (bit-identical)
# baseline (speedup 1.0000x reference)
; template <int MODE, int DQK, int DV>
; __device__ __forceinline__ void attn_pass(LAS unsigned char* lds, const Tens& T, size_t rowbase, int q0, f32x16 (&o)[DV / 32], float& l_out, const int wave, QPre* qp = nullptr) {
;     ...
;             if (active && !wdone) {
;                 const float csn = *(const LAS float*)(lds + OFF_CS + (sl * NSUB + sub) * 256 + 63 * 4) * LOG2E;
;                 if (__all((ct2 - csn) + bq < m - 32.0f)) wdone = true;
;             }
;             active = active && !wdone;
;         }
;         if (active) {
;             u32x2 mw = {0u, 0u};
;             if (MODE == AM_DSA) mw = *(const LAS u32x2*)(lds + OFF_MW + (sl * NSUB + sub) * 2048 + (wave * 32 + r) * 8);
;             f32x16 p[2];
;             const int kbase = 64 * j;
;             const bool diag = (kbase + 63 > q0 + wave * 32);
;             const bool nearb = (kbase + 63 + 128 > q0 + wave * 32);
;             constexpr bool POSTHOC = (MODE != AM_FOX);
;             constexpr float BIG = 65536.0f;
;             bool redo = (it == 0);
;             float psum;
;             for (;;) {
; #pragma unroll
;             for (int kb = 0; kb < 2; ++kb) {
;                 if (MODE == AM_FOX) {
;                     const float ctm = ct2 - m;
; #pragma unroll
;                     for (int g = 0; g < 4; ++g) {
;                         const f32x4 c = *(const LAS f32x4*)(lds + OFF_CS + (sl * NSUB + sub) * 256 + (32 * kb + 8 * g + 4 * h) * 4);
;                         p[kb][4 * g + 0] = fmaf(-LOG2E, c.x, ctm); p[kb][4 * g + 1] = fmaf(-LOG2E, c.y, ctm); p[kb][4 * g + 2] = fmaf(-LOG2E, c.z, ctm); p[kb][4 * g + 3] = fmaf(-LOG2E, c.w, ctm);
;                     }
;                 } else if (MODE == AM_DSA) {
; #pragma unroll
;                     for (int g = 0; g < 4; ++g) {
;                         const unsigned nib = __builtin_amdgcn_ubfe(mw[kb], (unsigned)(8 * g + 4 * h), 4u);
;                         const f32x4 t4 = *(const LAS f32x4*)(lds + OFF_LUT + 768 + nib * 16);
;                         p[kb][4 * g + 0] = t4.x; p[kb][4 * g + 1] = t4.y; p[kb][4 * g + 2] = t4.z; p[kb][4 * g + 3] = t4.w;
;                     }
;                     p[kb] = __builtin_amdgcn_mfma_f32_32x32x16_bf16(kone, qm, p[kb], 0, 0, 0);
;                 }
; #pragma unroll
;                 for (int s = 0; s < NSTEP; ++s) {
;                     bf16x8 a;
.LBB0_643:
	s_add_i32 s1, s46, 2
	s_cmp_gt_i32 s1, s94
	s_cbranch_scc1 .LBB0_650
	s_bitcmp1_b32 s12, 0
	s_cselect_b64 s[6:7], -1, 0
	s_mov_b32 s12, 1
	s_and_b64 vcc, exec, s[6:7]
	s_cbranch_vccnz .LBB0_650
	ds_read_b32 v32, v83 offset:49404
	s_waitcnt lgkmcnt(0)
	v_fmamk_f32 v86, v32, 0xbfb8aa3b, v104
	v_add_f32_e32 v32, v88, v86
	v_add_f32_e32 v33, v89, v87
	s_nop 0
	v_cmp_lt_f32_e32 vcc, v32, v33
	s_cmp_eq_u64 vcc, exec
	s_cbranch_scc1 .LBB0_650
	v_add_u32_e32 v60, 0, v82
	ds_read_b128 v[32:35], v60 offset:49152
	ds_read_b128 v[36:39], v60 offset:49184
	ds_read_b128 v[40:43], v60 offset:49216
	ds_read_b128 v[44:47], v60 offset:49248
	ds_read_b128 v[48:51], v95
	v_sub_f32_e32 v86, v104, v89
	s_waitcnt lgkmcnt(3)
	v_fma_f32 v36, v36, s64, v86
	v_fma_f32 v37, v37, s64, v86
	s_waitcnt lgkmcnt(2)
	v_fma_f32 v40, v40, s64, v86
	v_fma_f32 v41, v41, s64, v86
	s_waitcnt lgkmcnt(1)
	v_fma_f32 v44, v44, s64, v86
	v_fma_f32 v45, v45, s64, v86
	v_fma_f32 v32, v32, s64, v86
	v_fma_f32 v33, v33, s64, v86
	v_fma_f32 v46, v46, s64, v86
	v_fma_f32 v47, v47, s64, v86
	v_fma_f32 v42, v42, s64, v86
	v_fma_f32 v43, v43, s64, v86
	v_fma_f32 v38, v38, s64, v86
	v_fma_f32 v39, v39, s64, v86
	v_fma_f32 v34, v34, s64, v86
	v_fma_f32 v35, v35, s64, v86
	s_add_i32 s1, s0, 0x80
	s_cmp_le_i32 s1, s82
	s_waitcnt lgkmcnt(0)
	v_mfma_f32_32x32x16_bf16 v[32:47], v[48:51], v[64:67], v[32:47]
	ds_read_b128 v[48:51], v96
	s_waitcnt lgkmcnt(0)
	v_mfma_f32_32x32x16_bf16 v[32:47], v[48:51], v[68:71], v[32:47]
	ds_read_b128 v[48:51], v97
	s_waitcnt lgkmcnt(0)
	v_mfma_f32_32x32x16_bf16 v[32:47], v[48:51], v[72:75], v[32:47]
	ds_read_b128 v[48:51], v98
	s_waitcnt lgkmcnt(0)
	v_mfma_f32_32x32x16_bf16 v[32:47], v[48:51], v[76:79], v[32:47]
	ds_read_b128 v[48:51], v60 offset:49280
	ds_read_b128 v[52:55], v60 offset:49312
	ds_read_b128 v[56:59], v60 offset:49344
	ds_read_b128 v[60:63], v60 offset:49376
	ds_read_b128 v[108:111], v95 offset:4096
	s_waitcnt lgkmcnt(4)
	v_fma_f32 v48, v48, s64, v86
	v_fma_f32 v49, v49, s64, v86
	s_waitcnt lgkmcnt(3)
	v_fma_f32 v52, v52, s64, v86
	v_fma_f32 v53, v53, s64, v86
	s_waitcnt lgkmcnt(2)
	v_fma_f32 v56, v56, s64, v86
	v_fma_f32 v57, v57, s64, v86
	s_waitcnt lgkmcnt(1)
	v_fma_f32 v60, v60, s64, v86
	v_fma_f32 v61, v61, s64, v86
	v_fma_f32 v62, v62, s64, v86
	v_fma_f32 v63, v63, s64, v86
	v_fma_f32 v58, v58, s64, v86
	v_fma_f32 v59, v59, s64, v86
	v_fma_f32 v54, v54, s64, v86
	v_fma_f32 v55, v55, s64, v86
	v_fma_f32 v50, v50, s64, v86
	v_fma_f32 v51, v51, s64, v86
	s_waitcnt lgkmcnt(0)
	s_nop 0
	v_mfma_f32_32x32x16_bf16 v[48:63], v[108:111], v[64:67], v[48:63]
	ds_read_b128 v[108:111], v96 offset:4096
	s_waitcnt lgkmcnt(0)
	v_mfma_f32_32x32x16_bf16 v[48:63], v[108:111], v[68:71], v[48:63]
	ds_read_b128 v[108:111], v97 offset:4096
	s_waitcnt lgkmcnt(0)
	v_mfma_f32_32x32x16_bf16 v[48:63], v[108:111], v[72:75], v[48:63]
	ds_read_b128 v[108:111], v98 offset:4096
	s_waitcnt lgkmcnt(0)
	v_mfma_f32_32x32x16_bf16 v[48:63], v[108:111], v[76:79], v[48:63]
	s_cbranch_scc1 .LBB0_648
	v_add_u32_e32 v86, 0xffffff80, v106
	s_nop 0
	v_cmp_gt_i32_e32 vcc, 0, v86
	v_cmp_gt_i32_e64 s[6:7], 1, v86
	s_and_b64 vcc, s[6:7], vcc
	v_cndmask_b32_e32 v32, v32, v92, vcc
	v_cmp_lt_i32_e32 vcc, 1, v86
	v_cmp_gt_i32_e64 s[34:35], 58, v86
	v_cmp_gt_i32_e64 s[36:37], 59, v86
	v_cndmask_b32_e32 v34, v92, v34, vcc
	v_cmp_lt_i32_e32 vcc, 2, v86
	v_cmp_gt_i32_e64 s[30:31], 57, v86
	s_and_b64 s[34:35], s[36:37], s[34:35]
	v_cndmask_b32_e32 v35, v92, v35, vcc
	v_cmp_lt_i32_e32 vcc, 7, v86
	v_cmp_gt_i32_e64 s[28:29], 56, v86
	s_and_b64 s[30:31], s[34:35], s[30:31]
	v_cndmask_b32_e32 v36, v92, v36, vcc
	v_cmp_lt_i32_e32 vcc, 8, v86
	v_cmp_gt_i32_e64 s[26:27], 51, v86
	s_and_b64 s[28:29], s[30:31], s[28:29]
	v_cndmask_b32_e32 v37, v92, v37, vcc
	v_cmp_lt_i32_e32 vcc, 9, v86
	v_cmp_gt_i32_e64 s[24:25], 50, v86
	s_and_b64 s[26:27], s[28:29], s[26:27]
	v_cndmask_b32_e32 v38, v92, v38, vcc
	v_cmp_lt_i32_e32 vcc, 10, v86
	v_cmp_gt_i32_e64 s[22:23], 49, v86
	s_and_b64 s[24:25], s[26:27], s[24:25]
	v_cndmask_b32_e32 v39, v92, v39, vcc
	v_cmp_lt_i32_e32 vcc, 15, v86
	v_cmp_gt_i32_e64 s[20:21], 48, v86
	s_and_b64 s[22:23], s[24:25], s[22:23]
	v_cndmask_b32_e32 v40, v92, v40, vcc
	v_cmp_lt_i32_e32 vcc, 16, v86
	v_cmp_gt_i32_e64 s[18:19], 43, v86
	s_and_b64 s[20:21], s[22:23], s[20:21]
	v_cndmask_b32_e32 v41, v92, v41, vcc
	v_cmp_lt_i32_e32 vcc, 17, v86
	v_cmp_gt_i32_e64 s[16:17], 42, v86
	s_and_b64 s[18:19], s[20:21], s[18:19]
	v_cndmask_b32_e32 v42, v92, v42, vcc
	v_cmp_lt_i32_e32 vcc, 18, v86
	v_cmp_gt_i32_e64 s[14:15], 41, v86
	s_and_b64 s[16:17], s[18:19], s[16:17]
	v_cndmask_b32_e32 v43, v92, v43, vcc
	v_cmp_lt_i32_e32 vcc, 23, v86
	v_cmp_gt_i32_e64 s[12:13], 40, v86
	s_and_b64 s[14:15], s[16:17], s[14:15]
	v_cndmask_b32_e32 v44, v92, v44, vcc
	v_cmp_lt_i32_e32 vcc, 24, v86
	v_cmp_gt_i32_e64 s[10:11], 35, v86
	s_and_b64 s[12:13], s[14:15], s[12:13]
	v_cndmask_b32_e32 v45, v92, v45, vcc
	v_cmp_lt_i32_e32 vcc, 25, v86
	v_cmp_gt_i32_e64 s[8:9], 34, v86
	s_and_b64 s[10:11], s[12:13], s[10:11]
	v_cndmask_b32_e64 v33, v33, v92, s[6:7]
	v_cndmask_b32_e32 v46, v92, v46, vcc
	v_cmp_lt_i32_e32 vcc, 26, v86
	v_cmp_gt_i32_e64 s[6:7], 33, v86
	s_and_b64 s[8:9], s[10:11], s[8:9]
	v_cndmask_b32_e32 v107, v92, v47, vcc
	v_cmp_gt_i32_e32 vcc, 32, v86
	s_and_b64 s[6:7], s[8:9], s[6:7]
	s_and_b64 vcc, s[6:7], vcc
	v_cndmask_b32_e64 v63, v63, v92, s[36:37]
	v_cndmask_b32_e64 v62, v62, v92, s[34:35]
	v_cndmask_b32_e64 v61, v61, v92, s[30:31]
	v_cndmask_b32_e64 v60, v60, v92, s[28:29]
	v_cndmask_b32_e64 v59, v59, v92, s[26:27]
	v_cndmask_b32_e64 v58, v58, v92, s[24:25]
	v_cndmask_b32_e64 v57, v57, v92, s[22:23]
	v_cndmask_b32_e64 v56, v56, v92, s[20:21]
	v_cndmask_b32_e64 v55, v55, v92, s[18:19]
	v_cndmask_b32_e64 v54, v54, v92, s[16:17]
	v_cndmask_b32_e64 v53, v53, v92, s[14:15]
	v_cndmask_b32_e64 v52, v52, v92, s[12:13]
	v_cndmask_b32_e64 v51, v51, v92, s[10:11]
	v_cndmask_b32_e64 v50, v50, v92, s[8:9]
	v_cndmask_b32_e64 v49, v49, v92, s[6:7]
	v_cndmask_b32_e32 v47, v47, v107, vcc
	v_cndmask_b32_e32 v48, v48, v92, vcc

; template <int MODE, int DQK, int DV>
; __device__ __forceinline__ void attn_pass(LAS unsigned char* lds, const Tens& T, size_t rowbase, int q0, f32x16 (&o)[DV / 32], float& l_out, const int wave, QPre* qp = nullptr) {
;     ...
;             if (active && !wdone) {
;                 const float csn = *(const LAS float*)(lds + OFF_CS + (sl * NSUB + sub) * 256 + 63 * 4) * LOG2E;
;                 if (__all((ct2 - csn) + bq < m - 32.0f)) wdone = true;
;             }
;             active = active && !wdone;
;         }
;         if (active) {
;             u32x2 mw = {0u, 0u};
;             if (MODE == AM_DSA) mw = *(const LAS u32x2*)(lds + OFF_MW + (sl * NSUB + sub) * 2048 + (wave * 32 + r) * 8);
;             f32x16 p[2];
;             const int kbase = 64 * j;
;             const bool diag = (kbase + 63 > q0 + wave * 32);
;             const bool nearb = (kbase + 63 + 128 > q0 + wave * 32);
;             constexpr bool POSTHOC = (MODE != AM_FOX);
;             constexpr float BIG = 65536.0f;
;             bool redo = (it == 0);
;             float psum;
;             for (;;) {
; #pragma unroll
;             for (int kb = 0; kb < 2; ++kb) {
;                 if (MODE == AM_FOX) {
;                     const float ctm = ct2 - m;
; #pragma unroll
;                     for (int g = 0; g < 4; ++g) {
;                         const f32x4 c = *(const LAS f32x4*)(lds + OFF_CS + (sl * NSUB + sub) * 256 + (32 * kb + 8 * g + 4 * h) * 4);
;                         p[kb][4 * g + 0] = fmaf(-LOG2E, c.x, ctm); p[kb][4 * g + 1] = fmaf(-LOG2E, c.y, ctm); p[kb][4 * g + 2] = fmaf(-LOG2E, c.z, ctm); p[kb][4 * g + 3] = fmaf(-LOG2E, c.w, ctm);
;                     }
;                 } else if (MODE == AM_DSA) {
; #pragma unroll
;                     for (int g = 0; g < 4; ++g) {
;                         const unsigned nib = __builtin_amdgcn_ubfe(mw[kb], (unsigned)(8 * g + 4 * h), 4u);
;                         const f32x4 t4 = *(const LAS f32x4*)(lds + OFF_LUT + 768 + nib * 16);
;                         p[kb][4 * g + 0] = t4.x; p[kb][4 * g + 1] = t4.y; p[kb][4 * g + 2] = t4.z; p[kb][4 * g + 3] = t4.w;
;                     }
;                     p[kb] = __builtin_amdgcn_mfma_f32_32x32x16_bf16(kone, qm, p[kb], 0, 0, 0);
;                 }
; #pragma unroll
;                 for (int s = 0; s < NSTEP; ++s) {
;                     bf16x8 a;
.LBB0_663:
	s_or_b64 exec, exec, s[6:7]
	s_add_i32 s6, s46, 1
	s_cmp_gt_i32 s6, s94
	s_cbranch_scc1 .LBB0_670
	s_bitcmp1_b32 s12, 0
	s_cselect_b64 s[6:7], -1, 0
	s_mov_b32 s12, 1
	s_and_b64 vcc, exec, s[6:7]
	s_cbranch_vccnz .LBB0_670
	ds_read_b32 v32, v83 offset:49660
	s_waitcnt lgkmcnt(0)
	v_fmamk_f32 v86, v32, 0xbfb8aa3b, v104
	v_add_f32_e32 v32, v88, v86
	v_add_f32_e32 v33, v89, v87
	s_nop 0
	v_cmp_lt_f32_e32 vcc, v32, v33
	s_cmp_eq_u64 vcc, exec
	s_cbranch_scc1 .LBB0_670
	v_add_u32_e32 v60, 0, v82
	ds_read_b128 v[32:35], v60 offset:49408
	ds_read_b128 v[36:39], v60 offset:49440
	ds_read_b128 v[40:43], v60 offset:49472
	ds_read_b128 v[44:47], v60 offset:49504
	ds_read_b128 v[48:51], v95 offset:8192
	v_sub_f32_e32 v86, v104, v89
	s_waitcnt lgkmcnt(3)
	v_fma_f32 v36, v36, s64, v86
	v_fma_f32 v37, v37, s64, v86
	s_waitcnt lgkmcnt(2)
	v_fma_f32 v40, v40, s64, v86
	v_fma_f32 v41, v41, s64, v86
	s_waitcnt lgkmcnt(1)
	v_fma_f32 v44, v44, s64, v86
	v_fma_f32 v45, v45, s64, v86
	v_fma_f32 v32, v32, s64, v86
	v_fma_f32 v33, v33, s64, v86
	v_fma_f32 v46, v46, s64, v86
	v_fma_f32 v47, v47, s64, v86
	v_fma_f32 v42, v42, s64, v86
	v_fma_f32 v43, v43, s64, v86
	v_fma_f32 v38, v38, s64, v86
	v_fma_f32 v39, v39, s64, v86
	v_fma_f32 v34, v34, s64, v86
	v_fma_f32 v35, v35, s64, v86
	s_add_i32 s6, s0, 64
	s_cmp_le_i32 s6, s82
	s_waitcnt lgkmcnt(0)
	v_mfma_f32_32x32x16_bf16 v[32:47], v[48:51], v[64:67], v[32:47]
	ds_read_b128 v[48:51], v96 offset:8192
	s_waitcnt lgkmcnt(0)
	v_mfma_f32_32x32x16_bf16 v[32:47], v[48:51], v[68:71], v[32:47]
	ds_read_b128 v[48:51], v97 offset:8192
	s_waitcnt lgkmcnt(0)
	v_mfma_f32_32x32x16_bf16 v[32:47], v[48:51], v[72:75], v[32:47]
	ds_read_b128 v[48:51], v98 offset:8192
	s_waitcnt lgkmcnt(0)
	v_mfma_f32_32x32x16_bf16 v[32:47], v[48:51], v[76:79], v[32:47]
	ds_read_b128 v[48:51], v60 offset:49536
	ds_read_b128 v[52:55], v60 offset:49568
	ds_read_b128 v[56:59], v60 offset:49600
	ds_read_b128 v[60:63], v60 offset:49632
	ds_read_b128 v[108:111], v95 offset:12288
	s_waitcnt lgkmcnt(4)
	v_fma_f32 v48, v48, s64, v86
	v_fma_f32 v49, v49, s64, v86
	s_waitcnt lgkmcnt(3)
	v_fma_f32 v52, v52, s64, v86
	v_fma_f32 v53, v53, s64, v86
	s_waitcnt lgkmcnt(2)
	v_fma_f32 v56, v56, s64, v86
	v_fma_f32 v57, v57, s64, v86
	s_waitcnt lgkmcnt(1)
	v_fma_f32 v60, v60, s64, v86
	v_fma_f32 v61, v61, s64, v86
	v_fma_f32 v62, v62, s64, v86
	v_fma_f32 v63, v63, s64, v86
	v_fma_f32 v58, v58, s64, v86
	v_fma_f32 v59, v59, s64, v86
	v_fma_f32 v54, v54, s64, v86
	v_fma_f32 v55, v55, s64, v86
	v_fma_f32 v50, v50, s64, v86
	v_fma_f32 v51, v51, s64, v86
	s_waitcnt lgkmcnt(0)
	s_nop 0
	v_mfma_f32_32x32x16_bf16 v[48:63], v[108:111], v[64:67], v[48:63]
	ds_read_b128 v[108:111], v96 offset:12288
	s_waitcnt lgkmcnt(0)
	v_mfma_f32_32x32x16_bf16 v[48:63], v[108:111], v[68:71], v[48:63]
	ds_read_b128 v[108:111], v97 offset:12288
	s_waitcnt lgkmcnt(0)
	v_mfma_f32_32x32x16_bf16 v[48:63], v[108:111], v[72:75], v[48:63]
	ds_read_b128 v[108:111], v98 offset:12288
	s_waitcnt lgkmcnt(0)
	v_mfma_f32_32x32x16_bf16 v[48:63], v[108:111], v[76:79], v[48:63]
	s_cbranch_scc1 .LBB0_668
	v_subrev_u32_e32 v86, 64, v106
	s_nop 0
	v_cmp_gt_i32_e32 vcc, 0, v86
	v_cmp_gt_i32_e64 s[6:7], 1, v86
	s_and_b64 vcc, s[6:7], vcc
	v_cndmask_b32_e32 v32, v32, v92, vcc
	v_cmp_lt_i32_e32 vcc, 1, v86
	v_cmp_gt_i32_e64 s[34:35], 58, v86
	v_cmp_gt_i32_e64 s[36:37], 59, v86
	v_cndmask_b32_e32 v34, v92, v34, vcc
	v_cmp_lt_i32_e32 vcc, 2, v86
	v_cmp_gt_i32_e64 s[30:31], 57, v86
	s_and_b64 s[34:35], s[36:37], s[34:35]
	v_cndmask_b32_e32 v35, v92, v35, vcc
	v_cmp_lt_i32_e32 vcc, 7, v86
	v_cmp_gt_i32_e64 s[28:29], 56, v86
	s_and_b64 s[30:31], s[34:35], s[30:31]
	v_cndmask_b32_e32 v36, v92, v36, vcc
	v_cmp_lt_i32_e32 vcc, 8, v86
	v_cmp_gt_i32_e64 s[26:27], 51, v86
	s_and_b64 s[28:29], s[30:31], s[28:29]
	v_cndmask_b32_e32 v37, v92, v37, vcc
	v_cmp_lt_i32_e32 vcc, 9, v86
	v_cmp_gt_i32_e64 s[24:25], 50, v86
	s_and_b64 s[26:27], s[28:29], s[26:27]
	v_cndmask_b32_e32 v38, v92, v38, vcc
	v_cmp_lt_i32_e32 vcc, 10, v86
	v_cmp_gt_i32_e64 s[22:23], 49, v86
	s_and_b64 s[24:25], s[26:27], s[24:25]
	v_cndmask_b32_e32 v39, v92, v39, vcc
	v_cmp_lt_i32_e32 vcc, 15, v86
	v_cmp_gt_i32_e64 s[20:21], 48, v86
	s_and_b64 s[22:23], s[24:25], s[22:23]
	v_cndmask_b32_e32 v40, v92, v40, vcc
	v_cmp_lt_i32_e32 vcc, 16, v86
	v_cmp_gt_i32_e64 s[18:19], 43, v86
	s_and_b64 s[20:21], s[22:23], s[20:21]
	v_cndmask_b32_e32 v41, v92, v41, vcc
	v_cmp_lt_i32_e32 vcc, 17, v86
	v_cmp_gt_i32_e64 s[16:17], 42, v86
	s_and_b64 s[18:19], s[20:21], s[18:19]
	v_cndmask_b32_e32 v42, v92, v42, vcc
	v_cmp_lt_i32_e32 vcc, 18, v86
	v_cmp_gt_i32_e64 s[14:15], 41, v86
	s_and_b64 s[16:17], s[18:19], s[16:17]
	v_cndmask_b32_e32 v43, v92, v43, vcc
	v_cmp_lt_i32_e32 vcc, 23, v86
	v_cmp_gt_i32_e64 s[12:13], 40, v86
	s_and_b64 s[14:15], s[16:17], s[14:15]
	v_cndmask_b32_e32 v44, v92, v44, vcc
	v_cmp_lt_i32_e32 vcc, 24, v86
	v_cmp_gt_i32_e64 s[10:11], 35, v86
	s_and_b64 s[12:13], s[14:15], s[12:13]
	v_cndmask_b32_e32 v45, v92, v45, vcc
	v_cmp_lt_i32_e32 vcc, 25, v86
	v_cmp_gt_i32_e64 s[8:9], 34, v86
	s_and_b64 s[10:11], s[12:13], s[10:11]
	v_cndmask_b32_e64 v33, v33, v92, s[6:7]
	v_cndmask_b32_e32 v46, v92, v46, vcc
	v_cmp_lt_i32_e32 vcc, 26, v86
	v_cmp_gt_i32_e64 s[6:7], 33, v86
	s_and_b64 s[8:9], s[10:11], s[8:9]
	v_cndmask_b32_e32 v107, v92, v47, vcc
	v_cmp_gt_i32_e32 vcc, 32, v86
	s_and_b64 s[6:7], s[8:9], s[6:7]
	s_and_b64 vcc, s[6:7], vcc
	v_cndmask_b32_e64 v63, v63, v92, s[36:37]
	v_cndmask_b32_e64 v62, v62, v92, s[34:35]
	v_cndmask_b32_e64 v61, v61, v92, s[30:31]
	v_cndmask_b32_e64 v60, v60, v92, s[28:29]
	v_cndmask_b32_e64 v59, v59, v92, s[26:27]
	v_cndmask_b32_e64 v58, v58, v92, s[24:25]
	v_cndmask_b32_e64 v57, v57, v92, s[22:23]
	v_cndmask_b32_e64 v56, v56, v92, s[20:21]
	v_cndmask_b32_e64 v55, v55, v92, s[18:19]
	v_cndmask_b32_e64 v54, v54, v92, s[16:17]
	v_cndmask_b32_e64 v53, v53, v92, s[14:15]
	v_cndmask_b32_e64 v52, v52, v92, s[12:13]
	v_cndmask_b32_e64 v51, v51, v92, s[10:11]
	v_cndmask_b32_e64 v50, v50, v92, s[8:9]
	v_cndmask_b32_e64 v49, v49, v92, s[6:7]
	v_cndmask_b32_e32 v47, v47, v107, vcc
	v_cndmask_b32_e32 v48, v48, v92, vcc

; template <int MODE, int DQK, int DV>
; __device__ __forceinline__ void attn_pass(LAS unsigned char* lds, const Tens& T, size_t rowbase, int q0, f32x16 (&o)[DV / 32], float& l_out, const int wave, QPre* qp = nullptr) {
;     ...
;             if (active && !wdone) {
;                 const float csn = *(const LAS float*)(lds + OFF_CS + (sl * NSUB + sub) * 256 + 63 * 4) * LOG2E;
;                 if (__all((ct2 - csn) + bq < m - 32.0f)) wdone = true;
;             }
;             active = active && !wdone;
;         }
;         if (active) {
;             u32x2 mw = {0u, 0u};
;             if (MODE == AM_DSA) mw = *(const LAS u32x2*)(lds + OFF_MW + (sl * NSUB + sub) * 2048 + (wave * 32 + r) * 8);
;             f32x16 p[2];
;             const int kbase = 64 * j;
;             const bool diag = (kbase + 63 > q0 + wave * 32);
;             const bool nearb = (kbase + 63 + 128 > q0 + wave * 32);
;             constexpr bool POSTHOC = (MODE != AM_FOX);
;             constexpr float BIG = 65536.0f;
;             bool redo = (it == 0);
;             float psum;
;             for (;;) {
; #pragma unroll
;             for (int kb = 0; kb < 2; ++kb) {
;                 if (MODE == AM_FOX) {
;                     const float ctm = ct2 - m;
; #pragma unroll
;                     for (int g = 0; g < 4; ++g) {
;                         const f32x4 c = *(const LAS f32x4*)(lds + OFF_CS + (sl * NSUB + sub) * 256 + (32 * kb + 8 * g + 4 * h) * 4);
;                         p[kb][4 * g + 0] = fmaf(-LOG2E, c.x, ctm); p[kb][4 * g + 1] = fmaf(-LOG2E, c.y, ctm); p[kb][4 * g + 2] = fmaf(-LOG2E, c.z, ctm); p[kb][4 * g + 3] = fmaf(-LOG2E, c.w, ctm);
;                     }
;                 } else if (MODE == AM_DSA) {
; #pragma unroll
;                     for (int g = 0; g < 4; ++g) {
;                         const unsigned nib = __builtin_amdgcn_ubfe(mw[kb], (unsigned)(8 * g + 4 * h), 4u);
;                         const f32x4 t4 = *(const LAS f32x4*)(lds + OFF_LUT + 768 + nib * 16);
;                         p[kb][4 * g + 0] = t4.x; p[kb][4 * g + 1] = t4.y; p[kb][4 * g + 2] = t4.z; p[kb][4 * g + 3] = t4.w;
;                     }
;                     p[kb] = __builtin_amdgcn_mfma_f32_32x32x16_bf16(kone, qm, p[kb], 0, 0, 0);
;                 }
; #pragma unroll
;                 for (int s = 0; s < NSTEP; ++s) {
;                     bf16x8 a;
.LBB0_678:
	s_cmp_gt_i32 s46, s94
	s_cbranch_scc1 .LBB0_685
	s_bitcmp1_b32 s12, 0
	s_cselect_b64 s[6:7], -1, 0
	s_mov_b32 s12, 1
	s_and_b64 vcc, exec, s[6:7]
	s_cbranch_vccnz .LBB0_685
	ds_read_b32 v32, v83 offset:49916
	s_waitcnt lgkmcnt(0)
	v_fmamk_f32 v86, v32, 0xbfb8aa3b, v104
	v_add_f32_e32 v32, v88, v86
	v_add_f32_e32 v33, v89, v87
	s_nop 0
	v_cmp_lt_f32_e32 vcc, v32, v33
	s_cmp_eq_u64 vcc, exec
	s_cbranch_scc1 .LBB0_685
	v_add_u32_e32 v60, 0, v82
	ds_read_b128 v[32:35], v60 offset:49664
	ds_read_b128 v[36:39], v60 offset:49696
	ds_read_b128 v[40:43], v60 offset:49728
	ds_read_b128 v[44:47], v60 offset:49760
	ds_read_b128 v[48:51], v95 offset:16384
	v_sub_f32_e32 v86, v104, v89
	s_waitcnt lgkmcnt(3)
	v_fma_f32 v36, v36, s64, v86
	v_fma_f32 v37, v37, s64, v86
	s_waitcnt lgkmcnt(2)
	v_fma_f32 v40, v40, s64, v86
	v_fma_f32 v41, v41, s64, v86
	s_waitcnt lgkmcnt(1)
	v_fma_f32 v44, v44, s64, v86
	v_fma_f32 v45, v45, s64, v86
	v_fma_f32 v32, v32, s64, v86
	v_fma_f32 v33, v33, s64, v86
	v_fma_f32 v46, v46, s64, v86
	v_fma_f32 v47, v47, s64, v86
	v_fma_f32 v42, v42, s64, v86
	v_fma_f32 v43, v43, s64, v86
	v_fma_f32 v38, v38, s64, v86
	v_fma_f32 v39, v39, s64, v86
	v_fma_f32 v34, v34, s64, v86
	v_fma_f32 v35, v35, s64, v86
	s_cmp_le_i32 s0, s82
	s_waitcnt lgkmcnt(0)
	v_mfma_f32_32x32x16_bf16 v[32:47], v[48:51], v[64:67], v[32:47]
	ds_read_b128 v[48:51], v96 offset:16384
	s_waitcnt lgkmcnt(0)
	v_mfma_f32_32x32x16_bf16 v[32:47], v[48:51], v[68:71], v[32:47]
	ds_read_b128 v[48:51], v97 offset:16384
	s_waitcnt lgkmcnt(0)
	v_mfma_f32_32x32x16_bf16 v[32:47], v[48:51], v[72:75], v[32:47]
	ds_read_b128 v[48:51], v98 offset:16384
	s_waitcnt lgkmcnt(0)
	v_mfma_f32_32x32x16_bf16 v[32:47], v[48:51], v[76:79], v[32:47]
	ds_read_b128 v[48:51], v60 offset:49792
	ds_read_b128 v[52:55], v60 offset:49824
	ds_read_b128 v[56:59], v60 offset:49856
	ds_read_b128 v[60:63], v60 offset:49888
	ds_read_b128 v[108:111], v95 offset:20480
	s_waitcnt lgkmcnt(4)
	v_fma_f32 v48, v48, s64, v86
	v_fma_f32 v49, v49, s64, v86
	s_waitcnt lgkmcnt(3)
	v_fma_f32 v52, v52, s64, v86
	v_fma_f32 v53, v53, s64, v86
	s_waitcnt lgkmcnt(2)
	v_fma_f32 v56, v56, s64, v86
	v_fma_f32 v57, v57, s64, v86
	s_waitcnt lgkmcnt(1)
	v_fma_f32 v60, v60, s64, v86
	v_fma_f32 v61, v61, s64, v86
	v_fma_f32 v62, v62, s64, v86
	v_fma_f32 v63, v63, s64, v86
	v_fma_f32 v58, v58, s64, v86
	v_fma_f32 v59, v59, s64, v86
	v_fma_f32 v54, v54, s64, v86
	v_fma_f32 v55, v55, s64, v86
	v_fma_f32 v50, v50, s64, v86
	v_fma_f32 v51, v51, s64, v86
	s_waitcnt lgkmcnt(0)
	s_nop 0
	v_mfma_f32_32x32x16_bf16 v[48:63], v[108:111], v[64:67], v[48:63]
	ds_read_b128 v[108:111], v96 offset:20480
	s_waitcnt lgkmcnt(0)
	v_mfma_f32_32x32x16_bf16 v[48:63], v[108:111], v[68:71], v[48:63]
	ds_read_b128 v[108:111], v97 offset:20480
	s_waitcnt lgkmcnt(0)
	v_mfma_f32_32x32x16_bf16 v[48:63], v[108:111], v[72:75], v[48:63]
	ds_read_b128 v[108:111], v98 offset:20480
	s_waitcnt lgkmcnt(0)
	v_mfma_f32_32x32x16_bf16 v[48:63], v[108:111], v[76:79], v[48:63]
	s_cbranch_scc1 .LBB0_683
	v_mov_b32_e32 v86, v106
	s_nop 0
	v_cmp_gt_i32_e32 vcc, 0, v86
	v_cmp_gt_i32_e64 s[6:7], 1, v86
	s_and_b64 vcc, s[6:7], vcc
	v_cndmask_b32_e32 v32, v32, v92, vcc
	v_cmp_lt_i32_e32 vcc, 1, v86
	v_cmp_gt_i32_e64 s[34:35], 58, v86
	v_cmp_gt_i32_e64 s[36:37], 59, v86
	v_cndmask_b32_e32 v34, v92, v34, vcc
	v_cmp_lt_i32_e32 vcc, 2, v86
	v_cmp_gt_i32_e64 s[30:31], 57, v86
	s_and_b64 s[34:35], s[36:37], s[34:35]
	v_cndmask_b32_e32 v35, v92, v35, vcc
	v_cmp_lt_i32_e32 vcc, 7, v86
	v_cmp_gt_i32_e64 s[28:29], 56, v86
	s_and_b64 s[30:31], s[34:35], s[30:31]
	v_cndmask_b32_e32 v36, v92, v36, vcc
	v_cmp_lt_i32_e32 vcc, 8, v86
	v_cmp_gt_i32_e64 s[26:27], 51, v86
	s_and_b64 s[28:29], s[30:31], s[28:29]
	v_cndmask_b32_e32 v37, v92, v37, vcc
	v_cmp_lt_i32_e32 vcc, 9, v86
	v_cmp_gt_i32_e64 s[24:25], 50, v86
	s_and_b64 s[26:27], s[28:29], s[26:27]
	v_cndmask_b32_e32 v38, v92, v38, vcc
	v_cmp_lt_i32_e32 vcc, 10, v86
	v_cmp_gt_i32_e64 s[22:23], 49, v86
	s_and_b64 s[24:25], s[26:27], s[24:25]
	v_cndmask_b32_e32 v39, v92, v39, vcc
	v_cmp_lt_i32_e32 vcc, 15, v86
	v_cmp_gt_i32_e64 s[20:21], 48, v86
	s_and_b64 s[22:23], s[24:25], s[22:23]
	v_cndmask_b32_e32 v40, v92, v40, vcc
	v_cmp_lt_i32_e32 vcc, 16, v86
	v_cmp_gt_i32_e64 s[18:19], 43, v86
	s_and_b64 s[20:21], s[22:23], s[20:21]
	v_cndmask_b32_e32 v41, v92, v41, vcc
	v_cmp_lt_i32_e32 vcc, 17, v86
	v_cmp_gt_i32_e64 s[16:17], 42, v86
	s_and_b64 s[18:19], s[20:21], s[18:19]
	v_cndmask_b32_e32 v42, v92, v42, vcc
	v_cmp_lt_i32_e32 vcc, 18, v86
	v_cmp_gt_i32_e64 s[14:15], 41, v86
	s_and_b64 s[16:17], s[18:19], s[16:17]
	v_cndmask_b32_e32 v43, v92, v43, vcc
	v_cmp_lt_i32_e32 vcc, 23, v86
	v_cmp_gt_i32_e64 s[12:13], 40, v86
	s_and_b64 s[14:15], s[16:17], s[14:15]
	v_cndmask_b32_e32 v44, v92, v44, vcc
	v_cmp_lt_i32_e32 vcc, 24, v86
	v_cmp_gt_i32_e64 s[10:11], 35, v86
	s_and_b64 s[12:13], s[14:15], s[12:13]
	v_cndmask_b32_e32 v45, v92, v45, vcc
	v_cmp_lt_i32_e32 vcc, 25, v86
	v_cmp_gt_i32_e64 s[8:9], 34, v86
	s_and_b64 s[10:11], s[12:13], s[10:11]
	v_cndmask_b32_e64 v33, v33, v92, s[6:7]
	v_cndmask_b32_e32 v46, v92, v46, vcc
	v_cmp_lt_i32_e32 vcc, 26, v86
	v_cmp_gt_i32_e64 s[6:7], 33, v86
	s_and_b64 s[8:9], s[10:11], s[8:9]
	v_cndmask_b32_e32 v107, v92, v47, vcc
	v_cmp_gt_i32_e32 vcc, 32, v86
	s_and_b64 s[6:7], s[8:9], s[6:7]
	s_and_b64 vcc, s[6:7], vcc
	v_cndmask_b32_e64 v63, v63, v92, s[36:37]
	v_cndmask_b32_e64 v62, v62, v92, s[34:35]
	v_cndmask_b32_e64 v61, v61, v92, s[30:31]
	v_cndmask_b32_e64 v60, v60, v92, s[28:29]
	v_cndmask_b32_e64 v59, v59, v92, s[26:27]
	v_cndmask_b32_e64 v58, v58, v92, s[24:25]
	v_cndmask_b32_e64 v57, v57, v92, s[22:23]
	v_cndmask_b32_e64 v56, v56, v92, s[20:21]
	v_cndmask_b32_e64 v55, v55, v92, s[18:19]
	v_cndmask_b32_e64 v54, v54, v92, s[16:17]
	v_cndmask_b32_e64 v53, v53, v92, s[14:15]
	v_cndmask_b32_e64 v52, v52, v92, s[12:13]
	v_cndmask_b32_e64 v51, v51, v92, s[10:11]
	v_cndmask_b32_e64 v50, v50, v92, s[8:9]
	v_cndmask_b32_e64 v49, v49, v92, s[6:7]
	v_cndmask_b32_e32 v47, v47, v107, vcc
	v_cndmask_b32_e32 v48, v48, v92, vcc

; template <int MODE, int DQK, int DV>
; __device__ __forceinline__ void attn_pass(LAS unsigned char* lds, const Tens& T, size_t rowbase, int q0, f32x16 (&o)[DV / 32], float& l_out, const int wave, QPre* qp = nullptr) {
;     ...
;                 if (POSTHOC || __builtin_expect(__any(tmax > THR), 0)) {
;                     const float delta = fmaxf(tmax, 0.f);
;                     m += delta;
;                     const float alpha = __builtin_amdgcn_exp2f(-delta);
;                     l *= alpha;
; #pragma unroll
;                     for (int kb = 0; kb < 2; ++kb)
; #pragma unroll
;                         for (int rg = 0; rg < 16; ++rg) p[kb][rg] -= delta;
; #pragma unroll
;                     for (int i = 0; i < NDB; ++i)
; #pragma unroll
;                         for (int rg = 0; rg < 16; ++rg) o[i][rg] *= alpha;
.LBB0_708:
	v_mov_b32_e32 v108, v49
	v_max_f32_e32 v49, v86, v86
	v_mov_b32_e32 v109, v50
	v_mov_b32_e32 v50, v51
	v_mov_b32_e32 v51, v52
	v_mov_b32_e32 v52, v53
	v_mov_b32_e32 v53, v54
	v_mov_b32_e32 v54, v55
	v_mov_b32_e32 v55, v56
	v_mov_b32_e32 v56, v57
	v_mov_b32_e32 v57, v58
	v_mov_b32_e32 v58, v59
	v_mov_b32_e32 v59, v60
	v_max_f32_e32 v60, 0, v49
	v_exp_f32_e64 v86, -v60
	v_mov_b32_e32 v110, v61
	v_mov_b32_e32 v111, v62
	v_add_f32_e64 v108, v108, -v60
	v_add_f32_e64 v109, v109, -v60
	v_add_f32_e64 v112, v50, -v60
	v_add_f32_e64 v113, v51, -v60
	v_add_f32_e64 v114, v52, -v60
	v_add_f32_e64 v115, v53, -v60
	v_add_f32_e64 v116, v54, -v60
	v_add_f32_e64 v117, v55, -v60
	v_add_f32_e64 v118, v56, -v60
	v_add_f32_e64 v119, v57, -v60
	v_add_f32_e64 v120, v58, -v60
	v_add_f32_e64 v121, v59, -v60
	v_add_f32_e64 v110, v110, -v60
	v_add_f32_e64 v111, v111, -v60
	v_add_f32_e32 v89, v89, v60
	v_mul_f32_e32 v105, v105, v86
	v_sub_f32_e32 v32, v32, v60
	v_sub_f32_e32 v33, v33, v60
	v_add_f32_e64 v34, v34, -v60
	v_add_f32_e64 v35, v35, -v60
	v_add_f32_e64 v36, v36, -v60
	v_add_f32_e64 v37, v37, -v60
	v_add_f32_e64 v38, v38, -v60
	v_add_f32_e64 v39, v39, -v60
	v_add_f32_e64 v40, v40, -v60
	v_add_f32_e64 v41, v41, -v60
	v_add_f32_e64 v42, v42, -v60
	v_add_f32_e64 v43, v43, -v60
	v_add_f32_e64 v44, v44, -v60
	v_add_f32_e64 v45, v45, -v60
	v_add_f32_e64 v46, v46, -v60
	v_add_f32_e64 v47, v47, -v60
	v_sub_f32_e32 v48, v48, v60
	v_sub_f32_e32 v63, v63, v60
	v_mul_f32_e32 v30, v30, v86
	v_mul_f32_e32 v31, v31, v86
	v_mul_f32_e32 v28, v28, v86
	v_mul_f32_e32 v29, v29, v86
	v_mul_f32_e32 v26, v26, v86
	v_mul_f32_e32 v27, v27, v86
	v_mul_f32_e32 v24, v24, v86
	v_mul_f32_e32 v25, v25, v86
	v_mul_f32_e32 v22, v22, v86
	v_mul_f32_e32 v23, v23, v86
	v_mul_f32_e32 v20, v20, v86
	v_mul_f32_e32 v21, v21, v86
	v_mul_f32_e32 v18, v18, v86
	v_mul_f32_e32 v19, v19, v86
	v_mul_f32_e32 v16, v16, v86
	v_mul_f32_e32 v17, v17, v86
	v_mul_f32_e32 v14, v14, v86
	v_mul_f32_e32 v15, v15, v86
	v_mul_f32_e32 v12, v12, v86
	v_mul_f32_e32 v13, v13, v86
	v_mul_f32_e32 v10, v10, v86
	v_mul_f32_e32 v11, v11, v86
	v_mul_f32_e32 v8, v8, v86
	v_mul_f32_e32 v9, v9, v86
	v_mul_f32_e32 v6, v6, v86
	v_mul_f32_e32 v7, v7, v86
	v_mul_f32_e32 v4, v4, v86
	v_mul_f32_e32 v5, v5, v86
	v_mul_f32_e32 v2, v2, v86
	v_mul_f32_e32 v3, v3, v86
	v_mul_f32_e32 v0, v0, v86
	v_mul_f32_e32 v1, v1, v86
	v_mov_b32_e32 v49, v108
	v_mov_b32_e32 v50, v109
	v_mov_b32_e32 v51, v112
	v_mov_b32_e32 v52, v113
	v_mov_b32_e32 v53, v114
	v_mov_b32_e32 v54, v115
	v_mov_b32_e32 v55, v116
	v_mov_b32_e32 v56, v117
	v_mov_b32_e32 v57, v118
	v_mov_b32_e32 v58, v119
	v_mov_b32_e32 v59, v120
	v_mov_b32_e32 v60, v121
	v_mov_b32_e32 v61, v110
	v_mov_b32_e32 v62, v111
	s_branch .LBB0_649
